# conversion tail loads branched over (not issued at all) instead of exec-masked; flat barrier release kept
# baseline (speedup 1.0000x reference)
; __device__ __forceinline__ ConvJob conv_job(const Ctx& c, int t) {
;     ...
;     if (i < CV_IN) { const int kb = i % 16, cb = i / 16; j.src = c.in[4]; j.ld = NIN; j.k0 = kb * 128; j.col0 = cb * 128; j.dst = WSP(bf16, WS_WIN); j.dK = 2048; j.drow0 = cb * 128; return j; }
;     i -= CV_IN;
;     if (i < CV_OUT) { const int kb = i % 16, cb = i / 16; j.src = c.in[8]; j.ld = 2048; j.k0 = kb * 128; j.col0 = cb * 128; j.dst = WSP(bf16, WS_WOUT); j.dK = 2048; j.drow0 = cb * 128; return j; }
;     i -= CV_OUT;
;     if (i < CV_GLU) { const int kb = i % 16, cb = i / 16; j.src = c.in[17]; j.ld = 4096; j.k0 = kb * 128; j.col0 = cb * 128; j.dst = WSP(bf16, WS_WGLU); j.dK = 2048; j.drow0 = cb < 16 ? cb * 256 : (cb - 16) * 256 + 128; return j; }
;     i -= CV_GLU;
;     if (i < CV_GU) { const int kb = i % 16, cb = (i / 16) % 8, gu = (i / 128) % 2, le = i / 256;
;         j.src = (gu ? c.in[23] : c.in[22]) + (size_t)le * 2048 * 1024; j.ld = 1024; j.k0 = kb * 128; j.col0 = cb * 128; j.dst = WSP(bf16, WS_WGU) + (size_t)le * 2048 * 2048; j.dK = 2048; j.drow0 = cb * 256 + gu * 128; return j; }
;     i -= CV_GU;
;     { const int kb = i % 8, cb = (i / 8) % 16, le = i / 128;
;         j.src = c.in[24] + (size_t)le * 1024 * 2048; j.ld = 2048; j.k0 = kb * 128; j.col0 = cb * 128; j.dst = WSP(bf16, WS_WD) + (size_t)le * 2048 * 1024; j.dK = 1024; j.drow0 = cb * 128; return j; }
.LBB0_137:
	s_ashr_i32 s15, s14, 31
	s_lshl_b64 s[14:15], s[14:15], 2
	v_add_u32_e32 v5, s0, v9
	s_add_u32 s12, s12, s14
	v_ashrrev_i32_e32 v7, 31, v5
	s_addc_u32 s13, s13, s15
	v_mul_lo_u32 v7, s10, v7
	v_mul_lo_u32 v11, s11, v5
	v_mad_u64_u32 v[66:67], s[14:15], s10, v5, 0
	v_add3_u32 v67, v67, v7, v11
	v_lshl_add_u64 v[66:67], v[66:67], 2, s[12:13]
	v_add_u32_e32 v5, s0, v54
	s_mov_b32 m0, s29
	v_lshl_add_u64 v[66:67], v[66:67], 0, v[2:3]
	v_ashrrev_i32_e32 v7, 31, v5
	s_mov_b64 exec, s[98:99]
	s_cbranch_execz .Lcv_sk_0
	global_load_lds_dwordx4 v[66:67], off nt
.Lcv_sk_0:
	s_mov_b64 exec, s[100:101]
	v_mul_lo_u32 v7, s10, v7
	v_mul_lo_u32 v11, s11, v5
	v_mad_u64_u32 v[66:67], s[14:15], s10, v5, 0
	v_add3_u32 v67, v67, v7, v11
	v_lshl_add_u64 v[66:67], v[66:67], 2, s[12:13]
	v_mov_b32_e32 v5, v3
	v_lshl_add_u64 v[66:67], v[66:67], 0, v[4:5]
	v_add_u32_e32 v5, s0, v55
	s_mov_b32 m0, s30
	v_ashrrev_i32_e32 v7, 31, v5
	s_mov_b64 exec, s[98:99]
	s_cbranch_execz .Lcv_sk_1
	global_load_lds_dwordx4 v[66:67], off nt
.Lcv_sk_1:
	s_mov_b64 exec, s[100:101]
	v_mul_lo_u32 v7, s10, v7
	v_mul_lo_u32 v11, s11, v5
	v_mad_u64_u32 v[66:67], s[14:15], s10, v5, 0
	v_add3_u32 v67, v67, v7, v11
	v_lshl_add_u64 v[66:67], v[66:67], 2, s[12:13]
	v_mov_b32_e32 v7, v3
	v_add_u32_e32 v5, s0, v56
	v_lshl_add_u64 v[66:67], v[66:67], 0, v[6:7]
	s_mov_b32 m0, s31
	v_ashrrev_i32_e32 v7, 31, v5
	s_mov_b64 exec, s[98:99]
	s_cbranch_execz .Lcv_sk_2
	global_load_lds_dwordx4 v[66:67], off nt
.Lcv_sk_2:
	s_mov_b64 exec, s[100:101]
	v_mul_lo_u32 v7, s10, v7
	v_mul_lo_u32 v11, s11, v5
	v_mad_u64_u32 v[66:67], s[14:15], s10, v5, 0
	v_add3_u32 v67, v67, v7, v11
	v_lshl_add_u64 v[66:67], v[66:67], 2, s[12:13]
	v_mov_b32_e32 v11, v3
	v_add_u32_e32 v5, s0, v57
	v_lshl_add_u64 v[66:67], v[66:67], 0, v[10:11]
	s_mov_b32 m0, s33
	v_ashrrev_i32_e32 v7, 31, v5
	s_mov_b64 exec, s[98:99]
	s_cbranch_execz .Lcv_sk_3
	global_load_lds_dwordx4 v[66:67], off nt
.Lcv_sk_3:
	s_mov_b64 exec, s[100:101]
	v_mul_lo_u32 v7, s10, v7
	v_mul_lo_u32 v11, s11, v5
	v_mad_u64_u32 v[66:67], s[14:15], s10, v5, 0
	v_add3_u32 v67, v67, v7, v11
	v_lshl_add_u64 v[66:67], v[66:67], 2, s[12:13]
	v_mov_b32_e32 v13, v3
	v_add_u32_e32 v5, s0, v58
	v_lshl_add_u64 v[66:67], v[66:67], 0, v[12:13]
	s_mov_b32 m0, s97
	v_ashrrev_i32_e32 v7, 31, v5
	s_mov_b64 exec, s[98:99]
	s_cbranch_execz .Lcv_sk_4
	global_load_lds_dwordx4 v[66:67], off nt
.Lcv_sk_4:
	s_mov_b64 exec, s[100:101]
	v_mul_lo_u32 v7, s10, v7
	v_mul_lo_u32 v11, s11, v5
	v_mad_u64_u32 v[66:67], s[14:15], s10, v5, 0
	v_add3_u32 v67, v67, v7, v11
	v_lshl_add_u64 v[66:67], v[66:67], 2, s[12:13]
	v_mov_b32_e32 v15, v3
	v_add_u32_e32 v5, s0, v59
	v_lshl_add_u64 v[66:67], v[66:67], 0, v[14:15]
	s_mov_b32 m0, s79
	v_ashrrev_i32_e32 v7, 31, v5
	s_mov_b64 exec, s[98:99]
	s_cbranch_execz .Lcv_sk_5
	global_load_lds_dwordx4 v[66:67], off nt
.Lcv_sk_5:
	s_mov_b64 exec, s[100:101]
	v_mul_lo_u32 v7, s10, v7
	v_mul_lo_u32 v11, s11, v5
	v_mad_u64_u32 v[66:67], s[14:15], s10, v5, 0
	v_add3_u32 v67, v67, v7, v11
	v_lshl_add_u64 v[66:67], v[66:67], 2, s[12:13]
	v_mov_b32_e32 v17, v3
	v_add_u32_e32 v5, s0, v60
	v_lshl_add_u64 v[66:67], v[66:67], 0, v[16:17]
	s_mov_b32 m0, s19
	v_ashrrev_i32_e32 v7, 31, v5
	s_mov_b64 exec, s[98:99]
	s_cbranch_execz .Lcv_sk_6
	global_load_lds_dwordx4 v[66:67], off nt
.Lcv_sk_6:
	s_mov_b64 exec, s[100:101]
	v_mul_lo_u32 v7, s10, v7
	v_mul_lo_u32 v11, s11, v5
	v_mad_u64_u32 v[66:67], s[10:11], s10, v5, 0
	v_add3_u32 v67, v67, v7, v11
	v_lshl_add_u64 v[66:67], v[66:67], 2, s[12:13]
	v_mov_b32_e32 v19, v3
	v_lshl_add_u64 v[66:67], v[66:67], 0, v[18:19]
	s_add_i32 m0, s18, s27
	s_cmpk_lt_i32 s76, 0x480
	s_mov_b64 exec, s[98:99]
	s_cbranch_execz .Lcv_sk_7
	global_load_lds_dwordx4 v[66:67], off nt
.Lcv_sk_7:
	s_mov_b64 exec, s[100:101]
	s_cselect_b32 s11, 0, 0xfffffb80
	s_add_i32 s11, s11, s76
	s_cmpk_gt_i32 s11, 0x37f
	s_mov_b64 s[16:17], -1
	s_cbranch_scc0 .LBB0_151
	s_cmpk_gt_u32 s11, 0x47f
	s_cbranch_scc0 .LBB0_148
	s_cmpk_gt_u32 s11, 0x67f
	s_cbranch_scc0 .LBB0_145
	s_cmpk_gt_u32 s11, 0x467f
	s_mov_b64 s[12:13], -1
	s_cbranch_scc0 .LBB0_142
	s_add_i32 s0, s11, 0xffffb980
	s_lshr_b32 s0, s0, 7
	s_and_b32 s10, s44, 0x380
	s_and_b32 s18, s42, 0x780
	s_lshl_b64 s[12:13], s[0:1], 22
	v_readlane_b32 s0, v255, 3
	s_add_u32 s14, s0, s12
	v_readlane_b32 s0, v255, 4
	s_addc_u32 s15, s0, s13
	s_mov_b64 s[12:13], 0

; __device__ __forceinline__ ConvJob conv_job(const Ctx& c, int t) {
;     ...
;     if (i < CV_IN) { const int kb = i % 16, cb = i / 16; j.src = c.in[4]; j.ld = NIN; j.k0 = kb * 128; j.col0 = cb * 128; j.dst = WSP(bf16, WS_WIN); j.dK = 2048; j.drow0 = cb * 128; return j; }
;     i -= CV_IN;
;     if (i < CV_OUT) { const int kb = i % 16, cb = i / 16; j.src = c.in[8]; j.ld = 2048; j.k0 = kb * 128; j.col0 = cb * 128; j.dst = WSP(bf16, WS_WOUT); j.dK = 2048; j.drow0 = cb * 128; return j; }
;     i -= CV_OUT;
;     if (i < CV_GLU) { const int kb = i % 16, cb = i / 16; j.src = c.in[17]; j.ld = 4096; j.k0 = kb * 128; j.col0 = cb * 128; j.dst = WSP(bf16, WS_WGLU); j.dK = 2048; j.drow0 = cb < 16 ? cb * 256 : (cb - 16) * 256 + 128; return j; }
;     i -= CV_GLU;
;     if (i < CV_GU) { const int kb = i % 16, cb = (i / 16) % 8, gu = (i / 128) % 2, le = i / 256;
;         j.src = (gu ? c.in[23] : c.in[22]) + (size_t)le * 2048 * 1024; j.ld = 1024; j.k0 = kb * 128; j.col0 = cb * 128; j.dst = WSP(bf16, WS_WGU) + (size_t)le * 2048 * 2048; j.dK = 2048; j.drow0 = cb * 256 + gu * 128; return j; }
;     i -= CV_GU;
;     { const int kb = i % 8, cb = (i / 8) % 16, le = i / 128;
;         j.src = c.in[24] + (size_t)le * 1024 * 2048; j.ld = 2048; j.k0 = kb * 128; j.col0 = cb * 128; j.dst = WSP(bf16, WS_WD) + (size_t)le * 2048 * 1024; j.dK = 1024; j.drow0 = cb * 128; return j; }
.LBB0_357:
	s_ashr_i32 s21, s20, 31
	s_lshl_b64 s[20:21], s[20:21], 2
	v_add_u32_e32 v3, s10, v50
	s_add_u32 s18, s18, s20
	v_ashrrev_i32_e32 v5, 31, v3
	s_addc_u32 s19, s19, s21
	v_mul_lo_u32 v5, s16, v5
	v_mul_lo_u32 v7, s17, v3
	v_mad_u64_u32 v[64:65], s[20:21], s16, v3, 0
	v_add3_u32 v65, v65, v5, v7
	v_lshl_add_u64 v[64:65], v[64:65], 2, s[18:19]
	v_add_u32_e32 v3, s10, v51
	s_mov_b32 m0, s1
	v_lshl_add_u64 v[64:65], v[64:65], 0, v[0:1]
	v_ashrrev_i32_e32 v5, 31, v3
	s_mov_b64 exec, s[98:99]
	s_cbranch_execz .Lcv_sk_8
	global_load_lds_dwordx4 v[64:65], off nt
.Lcv_sk_8:
	s_mov_b64 exec, s[100:101]
	v_mul_lo_u32 v5, s16, v5
	v_mul_lo_u32 v7, s17, v3
	v_mad_u64_u32 v[64:65], s[20:21], s16, v3, 0
	v_add3_u32 v65, v65, v5, v7
	v_lshl_add_u64 v[64:65], v[64:65], 2, s[18:19]
	v_mov_b32_e32 v3, v1
	v_lshl_add_u64 v[64:65], v[64:65], 0, v[2:3]
	v_add_u32_e32 v3, s10, v52
	s_mov_b32 m0, s60
	v_ashrrev_i32_e32 v5, 31, v3
	s_mov_b64 exec, s[98:99]
	s_cbranch_execz .Lcv_sk_9
	global_load_lds_dwordx4 v[64:65], off nt
.Lcv_sk_9:
	s_mov_b64 exec, s[100:101]
	v_mul_lo_u32 v5, s16, v5
	v_mul_lo_u32 v7, s17, v3
	v_mad_u64_u32 v[64:65], s[20:21], s16, v3, 0
	v_add3_u32 v65, v65, v5, v7
	v_lshl_add_u64 v[64:65], v[64:65], 2, s[18:19]
	v_mov_b32_e32 v5, v1
	v_add_u32_e32 v3, s10, v53
	v_lshl_add_u64 v[64:65], v[64:65], 0, v[4:5]
	s_mov_b32 m0, s61
	v_ashrrev_i32_e32 v5, 31, v3
	s_mov_b64 exec, s[98:99]
	s_cbranch_execz .Lcv_sk_10
	global_load_lds_dwordx4 v[64:65], off nt
.Lcv_sk_10:
	s_mov_b64 exec, s[100:101]
	v_mul_lo_u32 v5, s16, v5
	v_mul_lo_u32 v7, s17, v3
	v_mad_u64_u32 v[64:65], s[20:21], s16, v3, 0
	v_add3_u32 v65, v65, v5, v7
	v_lshl_add_u64 v[64:65], v[64:65], 2, s[18:19]
	v_mov_b32_e32 v7, v1
	v_add_u32_e32 v3, s10, v54
	v_lshl_add_u64 v[64:65], v[64:65], 0, v[6:7]
	s_mov_b32 m0, s66
	v_ashrrev_i32_e32 v5, 31, v3
	s_mov_b64 exec, s[98:99]
	s_cbranch_execz .Lcv_sk_11
	global_load_lds_dwordx4 v[64:65], off nt
.Lcv_sk_11:
	s_mov_b64 exec, s[100:101]
	v_mul_lo_u32 v5, s16, v5
	v_mul_lo_u32 v7, s17, v3
	v_mad_u64_u32 v[64:65], s[20:21], s16, v3, 0
	v_add3_u32 v65, v65, v5, v7
	v_lshl_add_u64 v[64:65], v[64:65], 2, s[18:19]
	v_mov_b32_e32 v9, v1
	v_add_u32_e32 v3, s10, v55
	v_lshl_add_u64 v[64:65], v[64:65], 0, v[8:9]
	s_mov_b32 m0, s97
	v_ashrrev_i32_e32 v5, 31, v3
	s_mov_b64 exec, s[98:99]
	s_cbranch_execz .Lcv_sk_12
	global_load_lds_dwordx4 v[64:65], off nt
.Lcv_sk_12:
	s_mov_b64 exec, s[100:101]
	v_mul_lo_u32 v5, s16, v5
	v_mul_lo_u32 v7, s17, v3
	v_mad_u64_u32 v[64:65], s[20:21], s16, v3, 0
	v_add3_u32 v65, v65, v5, v7
	v_lshl_add_u64 v[64:65], v[64:65], 2, s[18:19]
	v_mov_b32_e32 v11, v1
	v_add_u32_e32 v3, s10, v56
	v_lshl_add_u64 v[64:65], v[64:65], 0, v[10:11]
	s_mov_b32 m0, s89
	v_ashrrev_i32_e32 v5, 31, v3
	s_mov_b64 exec, s[98:99]
	s_cbranch_execz .Lcv_sk_13
	global_load_lds_dwordx4 v[64:65], off nt
.Lcv_sk_13:
	s_mov_b64 exec, s[100:101]
	v_mul_lo_u32 v5, s16, v5
	v_mul_lo_u32 v7, s17, v3
	v_mad_u64_u32 v[64:65], s[20:21], s16, v3, 0
	v_add3_u32 v65, v65, v5, v7
	v_lshl_add_u64 v[64:65], v[64:65], 2, s[18:19]
	v_mov_b32_e32 v13, v1
	v_add_u32_e32 v3, s10, v57
	v_lshl_add_u64 v[64:65], v[64:65], 0, v[12:13]
	s_mov_b32 m0, s25
	v_ashrrev_i32_e32 v5, 31, v3
	s_mov_b64 exec, s[98:99]
	s_cbranch_execz .Lcv_sk_14
	global_load_lds_dwordx4 v[64:65], off nt
.Lcv_sk_14:
	s_mov_b64 exec, s[100:101]
	v_mul_lo_u32 v5, s16, v5
	v_mul_lo_u32 v7, s17, v3
	v_mad_u64_u32 v[64:65], s[16:17], s16, v3, 0
	v_add3_u32 v65, v65, v5, v7
	v_lshl_add_u64 v[64:65], v[64:65], 2, s[18:19]
	v_mov_b32_e32 v15, v1
	v_lshl_add_u64 v[64:65], v[64:65], 0, v[14:15]
	s_add_i32 m0, s24, s43
	s_cmpk_lt_i32 s84, 0x2200
	s_mov_b64 exec, s[98:99]
	s_cbranch_execz .Lcv_sk_15
	global_load_lds_dwordx4 v[64:65], off nt
.Lcv_sk_15:
	s_mov_b64 exec, s[100:101]
	s_cselect_b32 s17, s79, 0xffffde00
	s_add_i32 s17, s17, s84
	s_cmpk_gt_i32 s17, 0x37f
	s_mov_b64 s[22:23], -1
	s_cbranch_scc0 .LBB0_371
	s_cmpk_gt_u32 s17, 0x47f
	s_cbranch_scc0 .LBB0_368
	s_cmpk_gt_u32 s17, 0x67f
	s_cbranch_scc0 .LBB0_365
	s_cmpk_gt_u32 s17, 0x467f
	s_mov_b64 s[18:19], -1
	s_cbranch_scc0 .LBB0_362
	s_add_i32 s1, s17, 0xffffb980
	s_lshr_b32 s10, s1, 7
	s_and_b32 s16, s77, 0x380
	s_and_b32 s24, s75, 0x780
	s_lshl_b64 s[18:19], s[10:11], 22
	s_add_u32 s20, s71, s18
	s_addc_u32 s21, s72, s19
	s_mov_b64 s[18:19], 0

; __device__ __forceinline__ ConvJob conv_job(const Ctx& c, int t) {
;     ...
;     if (i < CV_IN) { const int kb = i % 16, cb = i / 16; j.src = c.in[4]; j.ld = NIN; j.k0 = kb * 128; j.col0 = cb * 128; j.dst = WSP(bf16, WS_WIN); j.dK = 2048; j.drow0 = cb * 128; return j; }
;     i -= CV_IN;
;     if (i < CV_OUT) { const int kb = i % 16, cb = i / 16; j.src = c.in[8]; j.ld = 2048; j.k0 = kb * 128; j.col0 = cb * 128; j.dst = WSP(bf16, WS_WOUT); j.dK = 2048; j.drow0 = cb * 128; return j; }
;     i -= CV_OUT;
;     if (i < CV_GLU) { const int kb = i % 16, cb = i / 16; j.src = c.in[17]; j.ld = 4096; j.k0 = kb * 128; j.col0 = cb * 128; j.dst = WSP(bf16, WS_WGLU); j.dK = 2048; j.drow0 = cb < 16 ? cb * 256 : (cb - 16) * 256 + 128; return j; }
;     i -= CV_GLU;
;     if (i < CV_GU) { const int kb = i % 16, cb = (i / 16) % 8, gu = (i / 128) % 2, le = i / 256;
;         j.src = (gu ? c.in[23] : c.in[22]) + (size_t)le * 2048 * 1024; j.ld = 1024; j.k0 = kb * 128; j.col0 = cb * 128; j.dst = WSP(bf16, WS_WGU) + (size_t)le * 2048 * 2048; j.dK = 2048; j.drow0 = cb * 256 + gu * 128; return j; }
;     i -= CV_GU;
;     { const int kb = i % 8, cb = (i / 8) % 16, le = i / 128;
;         j.src = c.in[24] + (size_t)le * 1024 * 2048; j.ld = 2048; j.k0 = kb * 128; j.col0 = cb * 128; j.dst = WSP(bf16, WS_WD) + (size_t)le * 2048 * 1024; j.dK = 1024; j.drow0 = cb * 128; return j; }
.LBB0_942:
	s_ashr_i32 s25, s24, 31
	s_lshl_b64 s[24:25], s[24:25], 2
	v_add_u32_e32 v3, s0, v50
	s_add_u32 s22, s22, s24
	v_ashrrev_i32_e32 v5, 31, v3
	s_addc_u32 s23, s23, s25
	v_mul_lo_u32 v5, s20, v5
	v_mul_lo_u32 v7, s21, v3
	v_mad_u64_u32 v[64:65], s[24:25], s20, v3, 0
	v_add3_u32 v65, v65, v5, v7
	v_lshl_add_u64 v[64:65], v[64:65], 2, s[22:23]
	v_add_u32_e32 v3, s0, v51
	s_mov_b32 m0, s69
	v_lshl_add_u64 v[64:65], v[64:65], 0, v[0:1]
	v_ashrrev_i32_e32 v5, 31, v3
	s_mov_b64 exec, s[98:99]
	s_cbranch_execz .Lcv_sk_16
	global_load_lds_dwordx4 v[64:65], off nt
.Lcv_sk_16:
	s_mov_b64 exec, s[100:101]
	v_mul_lo_u32 v5, s20, v5
	v_mul_lo_u32 v7, s21, v3
	v_mad_u64_u32 v[64:65], s[24:25], s20, v3, 0
	v_add3_u32 v65, v65, v5, v7
	v_lshl_add_u64 v[64:65], v[64:65], 2, s[22:23]
	v_mov_b32_e32 v3, v1
	v_lshl_add_u64 v[64:65], v[64:65], 0, v[2:3]
	v_add_u32_e32 v3, s0, v52
	s_mov_b32 m0, s70
	v_ashrrev_i32_e32 v5, 31, v3
	s_mov_b64 exec, s[98:99]
	s_cbranch_execz .Lcv_sk_17
	global_load_lds_dwordx4 v[64:65], off nt
.Lcv_sk_17:
	s_mov_b64 exec, s[100:101]
	v_mul_lo_u32 v5, s20, v5
	v_mul_lo_u32 v7, s21, v3
	v_mad_u64_u32 v[64:65], s[24:25], s20, v3, 0
	v_add3_u32 v65, v65, v5, v7
	v_lshl_add_u64 v[64:65], v[64:65], 2, s[22:23]
	v_mov_b32_e32 v5, v1
	v_add_u32_e32 v3, s0, v53
	v_lshl_add_u64 v[64:65], v[64:65], 0, v[4:5]
	s_mov_b32 m0, s97
	v_ashrrev_i32_e32 v5, 31, v3
	s_mov_b64 exec, s[98:99]
	s_cbranch_execz .Lcv_sk_18
	global_load_lds_dwordx4 v[64:65], off nt
.Lcv_sk_18:
	s_mov_b64 exec, s[100:101]
	v_mul_lo_u32 v5, s20, v5
	v_mul_lo_u32 v7, s21, v3
	v_mad_u64_u32 v[64:65], s[24:25], s20, v3, 0
	v_add3_u32 v65, v65, v5, v7
	v_lshl_add_u64 v[64:65], v[64:65], 2, s[22:23]
	v_mov_b32_e32 v7, v1
	v_add_u32_e32 v3, s0, v54
	v_lshl_add_u64 v[64:65], v[64:65], 0, v[6:7]
	s_mov_b32 m0, s89
	v_ashrrev_i32_e32 v5, 31, v3
	s_mov_b64 exec, s[98:99]
	s_cbranch_execz .Lcv_sk_19
	global_load_lds_dwordx4 v[64:65], off nt
.Lcv_sk_19:
	s_mov_b64 exec, s[100:101]
	v_mul_lo_u32 v5, s20, v5
	v_mul_lo_u32 v7, s21, v3
	v_mad_u64_u32 v[64:65], s[24:25], s20, v3, 0
	v_add3_u32 v65, v65, v5, v7
	v_lshl_add_u64 v[64:65], v[64:65], 2, s[22:23]
	v_mov_b32_e32 v9, v1
	v_add_u32_e32 v3, s0, v55
	v_lshl_add_u64 v[64:65], v[64:65], 0, v[8:9]
	s_mov_b32 m0, s88
	v_ashrrev_i32_e32 v5, 31, v3
	s_mov_b64 exec, s[98:99]
	s_cbranch_execz .Lcv_sk_20
	global_load_lds_dwordx4 v[64:65], off nt
.Lcv_sk_20:
	s_mov_b64 exec, s[100:101]
	v_mul_lo_u32 v5, s20, v5
	v_mul_lo_u32 v7, s21, v3
	v_mad_u64_u32 v[64:65], s[24:25], s20, v3, 0
	v_add3_u32 v65, v65, v5, v7
	v_lshl_add_u64 v[64:65], v[64:65], 2, s[22:23]
	v_mov_b32_e32 v11, v1
	v_add_u32_e32 v3, s0, v56
	v_lshl_add_u64 v[64:65], v[64:65], 0, v[10:11]
	s_mov_b32 m0, s85
	v_ashrrev_i32_e32 v5, 31, v3
	s_mov_b64 exec, s[98:99]
	s_cbranch_execz .Lcv_sk_21
	global_load_lds_dwordx4 v[64:65], off nt
.Lcv_sk_21:
	s_mov_b64 exec, s[100:101]
	v_mul_lo_u32 v5, s20, v5
	v_mul_lo_u32 v7, s21, v3
	v_mad_u64_u32 v[64:65], s[24:25], s20, v3, 0
	v_add3_u32 v65, v65, v5, v7
	v_lshl_add_u64 v[64:65], v[64:65], 2, s[22:23]
	v_mov_b32_e32 v13, v1
	v_add_u32_e32 v3, s0, v57
	v_lshl_add_u64 v[64:65], v[64:65], 0, v[12:13]
	s_mov_b32 m0, s29
	v_ashrrev_i32_e32 v5, 31, v3
	s_mov_b64 exec, s[98:99]
	s_cbranch_execz .Lcv_sk_22
	global_load_lds_dwordx4 v[64:65], off nt
.Lcv_sk_22:
	s_mov_b64 exec, s[100:101]
	v_mul_lo_u32 v5, s20, v5
	v_mul_lo_u32 v7, s21, v3
	v_mad_u64_u32 v[64:65], s[20:21], s20, v3, 0
	v_add3_u32 v65, v65, v5, v7
	v_lshl_add_u64 v[64:65], v[64:65], 2, s[22:23]
	v_mov_b32_e32 v15, v1
	v_lshl_add_u64 v[64:65], v[64:65], 0, v[14:15]
	s_add_i32 m0, s28, s80
	s_cmp_ge_i32 s36, s33
	s_mov_b64 exec, s[98:99]
	s_cbranch_execz .Lcv_sk_23
	global_load_lds_dwordx4 v[64:65], off nt
.Lcv_sk_23:
	s_mov_b64 exec, s[100:101]
	s_cselect_b32 s21, s38, 0x4680
	s_add_i32 s21, s21, s36
	s_cmpk_gt_i32 s21, 0x37f
	s_mov_b64 s[26:27], -1
	s_cbranch_scc0 .LBB0_956
	s_cmpk_gt_u32 s21, 0x47f
	s_cbranch_scc0 .LBB0_953
	s_cmpk_gt_u32 s21, 0x67f
	s_cbranch_scc0 .LBB0_950
	s_cmpk_gt_u32 s21, 0x467f
	s_mov_b64 s[22:23], -1
	s_cbranch_scc0 .LBB0_947
	s_add_i32 s0, s21, 0xffffb980
	s_lshr_b32 s0, s0, 7
	s_lshl_b32 s20, s21, 7
	s_lshl_b32 s22, s21, 4
	s_and_b32 s20, s20, 0x380
	s_and_b32 s28, s22, 0x780
	s_lshl_b64 s[22:23], s[0:1], 22
	s_add_u32 s24, s81, s22
	s_addc_u32 s25, s82, s23
	s_mov_b64 s[22:23], 0

.LBB0_1044:
	s_ashr_i32 s25, s24, 31
	s_lshl_b64 s[24:25], s[24:25], 2
	v_add_u32_e32 v3, s0, v50
	s_add_u32 s22, s22, s24
	v_ashrrev_i32_e32 v5, 31, v3
	s_addc_u32 s23, s23, s25
	v_mul_lo_u32 v5, s20, v5
	v_mul_lo_u32 v7, s21, v3
	v_mad_u64_u32 v[64:65], s[24:25], s20, v3, 0
	v_add3_u32 v65, v65, v5, v7
	v_lshl_add_u64 v[64:65], v[64:65], 2, s[22:23]
	v_add_u32_e32 v3, s0, v51
	s_mov_b32 m0, s49
	v_lshl_add_u64 v[64:65], v[64:65], 0, v[0:1]
	v_ashrrev_i32_e32 v5, 31, v3
	s_mov_b64 exec, s[98:99]
	s_cbranch_execz .Lcv_sk_24
	global_load_lds_dwordx4 v[64:65], off nt
.Lcv_sk_24:
	s_mov_b64 exec, s[100:101]
	v_mul_lo_u32 v5, s20, v5
	v_mul_lo_u32 v7, s21, v3
	v_mad_u64_u32 v[64:65], s[24:25], s20, v3, 0
	v_add3_u32 v65, v65, v5, v7
	v_lshl_add_u64 v[64:65], v[64:65], 2, s[22:23]
	v_mov_b32_e32 v3, v1
	v_lshl_add_u64 v[64:65], v[64:65], 0, v[2:3]
	v_add_u32_e32 v3, s0, v52
	s_mov_b32 m0, s48
	v_ashrrev_i32_e32 v5, 31, v3
	s_mov_b64 exec, s[98:99]
	s_cbranch_execz .Lcv_sk_25
	global_load_lds_dwordx4 v[64:65], off nt
.Lcv_sk_25:
	s_mov_b64 exec, s[100:101]
	v_mul_lo_u32 v5, s20, v5
	v_mul_lo_u32 v7, s21, v3
	v_mad_u64_u32 v[64:65], s[24:25], s20, v3, 0
	v_add3_u32 v65, v65, v5, v7
	v_lshl_add_u64 v[64:65], v[64:65], 2, s[22:23]
	v_mov_b32_e32 v5, v1
	v_add_u32_e32 v3, s0, v53
	v_lshl_add_u64 v[64:65], v[64:65], 0, v[4:5]
	s_mov_b32 m0, s84
	v_ashrrev_i32_e32 v5, 31, v3
	s_mov_b64 exec, s[98:99]
	s_cbranch_execz .Lcv_sk_26
	global_load_lds_dwordx4 v[64:65], off nt
.Lcv_sk_26:
	s_mov_b64 exec, s[100:101]
	v_mul_lo_u32 v5, s20, v5
	v_mul_lo_u32 v7, s21, v3
	v_mad_u64_u32 v[64:65], s[24:25], s20, v3, 0
	v_add3_u32 v65, v65, v5, v7
	v_lshl_add_u64 v[64:65], v[64:65], 2, s[22:23]
	v_mov_b32_e32 v7, v1
	v_add_u32_e32 v3, s0, v54
	v_lshl_add_u64 v[64:65], v[64:65], 0, v[6:7]
	s_mov_b32 m0, s79
	v_ashrrev_i32_e32 v5, 31, v3
	s_mov_b64 exec, s[98:99]
	s_cbranch_execz .Lcv_sk_27
	global_load_lds_dwordx4 v[64:65], off nt
.Lcv_sk_27:
	s_mov_b64 exec, s[100:101]
	v_mul_lo_u32 v5, s20, v5
	v_mul_lo_u32 v7, s21, v3
	v_mad_u64_u32 v[64:65], s[24:25], s20, v3, 0
	v_add3_u32 v65, v65, v5, v7
	v_lshl_add_u64 v[64:65], v[64:65], 2, s[22:23]
	v_mov_b32_e32 v9, v1
	v_add_u32_e32 v3, s0, v55
	v_lshl_add_u64 v[64:65], v[64:65], 0, v[8:9]
	s_mov_b32 m0, s78
	v_ashrrev_i32_e32 v5, 31, v3
	s_mov_b64 exec, s[98:99]
	s_cbranch_execz .Lcv_sk_28
	global_load_lds_dwordx4 v[64:65], off nt
.Lcv_sk_28:
	s_mov_b64 exec, s[100:101]
	v_mul_lo_u32 v5, s20, v5
	v_mul_lo_u32 v7, s21, v3
	v_mad_u64_u32 v[64:65], s[24:25], s20, v3, 0
	v_add3_u32 v65, v65, v5, v7
	v_lshl_add_u64 v[64:65], v[64:65], 2, s[22:23]
	v_mov_b32_e32 v11, v1
	v_add_u32_e32 v3, s0, v56
	v_lshl_add_u64 v[64:65], v[64:65], 0, v[10:11]
	s_mov_b32 m0, s77
	v_ashrrev_i32_e32 v5, 31, v3
	s_mov_b64 exec, s[98:99]
	s_cbranch_execz .Lcv_sk_29
	global_load_lds_dwordx4 v[64:65], off nt

; __device__ __forceinline__ ConvJob conv_job(const Ctx& c, int t) {
;     ...
;     if (i < CV_IN) { const int kb = i % 16, cb = i / 16; j.src = c.in[4]; j.ld = NIN; j.k0 = kb * 128; j.col0 = cb * 128; j.dst = WSP(bf16, WS_WIN); j.dK = 2048; j.drow0 = cb * 128; return j; }
;     i -= CV_IN;
;     if (i < CV_OUT) { const int kb = i % 16, cb = i / 16; j.src = c.in[8]; j.ld = 2048; j.k0 = kb * 128; j.col0 = cb * 128; j.dst = WSP(bf16, WS_WOUT); j.dK = 2048; j.drow0 = cb * 128; return j; }
;     i -= CV_OUT;
;     if (i < CV_GLU) { const int kb = i % 16, cb = i / 16; j.src = c.in[17]; j.ld = 4096; j.k0 = kb * 128; j.col0 = cb * 128; j.dst = WSP(bf16, WS_WGLU); j.dK = 2048; j.drow0 = cb < 16 ? cb * 256 : (cb - 16) * 256 + 128; return j; }
;     i -= CV_GLU;
;     if (i < CV_GU) { const int kb = i % 16, cb = (i / 16) % 8, gu = (i / 128) % 2, le = i / 256;
;         j.src = (gu ? c.in[23] : c.in[22]) + (size_t)le * 2048 * 1024; j.ld = 1024; j.k0 = kb * 128; j.col0 = cb * 128; j.dst = WSP(bf16, WS_WGU) + (size_t)le * 2048 * 2048; j.dK = 2048; j.drow0 = cb * 256 + gu * 128; return j; }
;     i -= CV_GU;
;     { const int kb = i % 8, cb = (i / 8) % 16, le = i / 128;
;         j.src = c.in[24] + (size_t)le * 1024 * 2048; j.ld = 2048; j.k0 = kb * 128; j.col0 = cb * 128; j.dst = WSP(bf16, WS_WD) + (size_t)le * 2048 * 1024; j.dK = 1024; j.drow0 = cb * 128; return j; }
.Lcv_sk_30:
	s_mov_b64 exec, s[100:101]
	v_mul_lo_u32 v5, s20, v5
	v_mul_lo_u32 v7, s21, v3
	v_mad_u64_u32 v[64:65], s[20:21], s20, v3, 0
	v_add3_u32 v65, v65, v5, v7
	v_lshl_add_u64 v[64:65], v[64:65], 2, s[22:23]
	v_mov_b32_e32 v15, v1
	v_lshl_add_u64 v[64:65], v[64:65], 0, v[14:15]
	s_add_i32 m0, s28, s61
	s_cmp_lt_i32 s75, s34
	s_mov_b64 exec, s[98:99]
	s_cbranch_execz .Lcv_sk_31
	global_load_lds_dwordx4 v[64:65], off nt
.Lcv_sk_31:
	s_mov_b64 exec, s[100:101]
	s_cselect_b32 s21, s31, s33
	s_add_i32 s21, s21, s75
	s_cmpk_gt_i32 s21, 0x37f
	s_mov_b64 s[26:27], -1
	s_cbranch_scc0 .LBB0_1058
	s_cmpk_gt_u32 s21, 0x47f
	s_cbranch_scc0 .LBB0_1055
	s_cmpk_gt_u32 s21, 0x67f
	s_cbranch_scc0 .LBB0_1052
	s_cmpk_gt_u32 s21, 0x467f
	s_mov_b64 s[22:23], -1
	s_cbranch_scc0 .LBB0_1049
	s_add_i32 s0, s21, 0xffffb980
	s_lshr_b32 s0, s0, 7
	s_lshl_b32 s20, s21, 7
	s_lshl_b32 s22, s21, 4
	s_and_b32 s20, s20, 0x380
	s_and_b32 s28, s22, 0x780
	s_lshl_b64 s[22:23], s[0:1], 22
	s_add_u32 s24, s73, s22
	s_addc_u32 s25, s74, s23
	s_mov_b64 s[22:23], 0

; __device__ __forceinline__ ConvJob conv_job(const Ctx& c, int t) {
;     ...
;     if (i < CV_IN) { const int kb = i % 16, cb = i / 16; j.src = c.in[4]; j.ld = NIN; j.k0 = kb * 128; j.col0 = cb * 128; j.dst = WSP(bf16, WS_WIN); j.dK = 2048; j.drow0 = cb * 128; return j; }
;     i -= CV_IN;
;     if (i < CV_OUT) { const int kb = i % 16, cb = i / 16; j.src = c.in[8]; j.ld = 2048; j.k0 = kb * 128; j.col0 = cb * 128; j.dst = WSP(bf16, WS_WOUT); j.dK = 2048; j.drow0 = cb * 128; return j; }
;     i -= CV_OUT;
;     if (i < CV_GLU) { const int kb = i % 16, cb = i / 16; j.src = c.in[17]; j.ld = 4096; j.k0 = kb * 128; j.col0 = cb * 128; j.dst = WSP(bf16, WS_WGLU); j.dK = 2048; j.drow0 = cb < 16 ? cb * 256 : (cb - 16) * 256 + 128; return j; }
;     i -= CV_GLU;
;     if (i < CV_GU) { const int kb = i % 16, cb = (i / 16) % 8, gu = (i / 128) % 2, le = i / 256;
;         j.src = (gu ? c.in[23] : c.in[22]) + (size_t)le * 2048 * 1024; j.ld = 1024; j.k0 = kb * 128; j.col0 = cb * 128; j.dst = WSP(bf16, WS_WGU) + (size_t)le * 2048 * 2048; j.dK = 2048; j.drow0 = cb * 256 + gu * 128; return j; }
;     i -= CV_GU;
;     { const int kb = i % 8, cb = (i / 8) % 16, le = i / 128;
;         j.src = c.in[24] + (size_t)le * 1024 * 2048; j.ld = 2048; j.k0 = kb * 128; j.col0 = cb * 128; j.dst = WSP(bf16, WS_WD) + (size_t)le * 2048 * 1024; j.dK = 1024; j.drow0 = cb * 128; return j; }
.LBB0_1305:
	s_ashr_i32 s23, s22, 31
	s_lshl_b64 s[22:23], s[22:23], 2
	v_add_u32_e32 v3, s0, v50
	s_add_u32 s20, s20, s22
	v_ashrrev_i32_e32 v5, 31, v3
	s_addc_u32 s21, s21, s23
	v_mul_lo_u32 v5, s18, v5
	v_mul_lo_u32 v7, s19, v3
	v_mad_u64_u32 v[64:65], s[22:23], s18, v3, 0
	v_add3_u32 v65, v65, v5, v7
	v_lshl_add_u64 v[64:65], v[64:65], 2, s[20:21]
	v_add_u32_e32 v3, s0, v51
	s_mov_b32 m0, s69
	v_lshl_add_u64 v[64:65], v[64:65], 0, v[0:1]
	v_ashrrev_i32_e32 v5, 31, v3
	s_mov_b64 exec, s[98:99]
	s_cbranch_execz .Lcv_sk_32
	global_load_lds_dwordx4 v[64:65], off nt
.Lcv_sk_32:
	s_mov_b64 exec, s[100:101]
	v_mul_lo_u32 v5, s18, v5
	v_mul_lo_u32 v7, s19, v3
	v_mad_u64_u32 v[64:65], s[22:23], s18, v3, 0
	v_add3_u32 v65, v65, v5, v7
	v_lshl_add_u64 v[64:65], v[64:65], 2, s[20:21]
	v_mov_b32_e32 v3, v1
	v_lshl_add_u64 v[64:65], v[64:65], 0, v[2:3]
	v_add_u32_e32 v3, s0, v52
	s_mov_b32 m0, s70
	v_ashrrev_i32_e32 v5, 31, v3
	s_mov_b64 exec, s[98:99]
	s_cbranch_execz .Lcv_sk_33
	global_load_lds_dwordx4 v[64:65], off nt
.Lcv_sk_33:
	s_mov_b64 exec, s[100:101]
	v_mul_lo_u32 v5, s18, v5
	v_mul_lo_u32 v7, s19, v3
	v_mad_u64_u32 v[64:65], s[22:23], s18, v3, 0
	v_add3_u32 v65, v65, v5, v7
	v_lshl_add_u64 v[64:65], v[64:65], 2, s[20:21]
	v_mov_b32_e32 v5, v1
	v_add_u32_e32 v3, s0, v53
	v_lshl_add_u64 v[64:65], v[64:65], 0, v[4:5]
	s_mov_b32 m0, s97
	v_ashrrev_i32_e32 v5, 31, v3
	s_mov_b64 exec, s[98:99]
	s_cbranch_execz .Lcv_sk_34
	global_load_lds_dwordx4 v[64:65], off nt
.Lcv_sk_34:
	s_mov_b64 exec, s[100:101]
	v_mul_lo_u32 v5, s18, v5
	v_mul_lo_u32 v7, s19, v3
	v_mad_u64_u32 v[64:65], s[22:23], s18, v3, 0
	v_add3_u32 v65, v65, v5, v7
	v_lshl_add_u64 v[64:65], v[64:65], 2, s[20:21]
	v_mov_b32_e32 v7, v1
	v_add_u32_e32 v3, s0, v54
	v_lshl_add_u64 v[64:65], v[64:65], 0, v[6:7]
	s_mov_b32 m0, s89
	v_ashrrev_i32_e32 v5, 31, v3
	s_mov_b64 exec, s[98:99]
	s_cbranch_execz .Lcv_sk_35
	global_load_lds_dwordx4 v[64:65], off nt
.Lcv_sk_35:
	s_mov_b64 exec, s[100:101]
	v_mul_lo_u32 v5, s18, v5
	v_mul_lo_u32 v7, s19, v3
	v_mad_u64_u32 v[64:65], s[22:23], s18, v3, 0
	v_add3_u32 v65, v65, v5, v7
	v_lshl_add_u64 v[64:65], v[64:65], 2, s[20:21]
	v_mov_b32_e32 v9, v1
	v_add_u32_e32 v3, s0, v55
	v_lshl_add_u64 v[64:65], v[64:65], 0, v[8:9]
	s_mov_b32 m0, s88
	v_ashrrev_i32_e32 v5, 31, v3
	s_mov_b64 exec, s[98:99]
	s_cbranch_execz .Lcv_sk_36
	global_load_lds_dwordx4 v[64:65], off nt
.Lcv_sk_36:
	s_mov_b64 exec, s[100:101]
	v_mul_lo_u32 v5, s18, v5
	v_mul_lo_u32 v7, s19, v3
	v_mad_u64_u32 v[64:65], s[22:23], s18, v3, 0
	v_add3_u32 v65, v65, v5, v7
	v_lshl_add_u64 v[64:65], v[64:65], 2, s[20:21]
	v_mov_b32_e32 v11, v1
	v_add_u32_e32 v3, s0, v56
	v_lshl_add_u64 v[64:65], v[64:65], 0, v[10:11]
	s_mov_b32 m0, s85
	v_ashrrev_i32_e32 v5, 31, v3
	s_mov_b64 exec, s[98:99]
	s_cbranch_execz .Lcv_sk_37
	global_load_lds_dwordx4 v[64:65], off nt
.Lcv_sk_37:
	s_mov_b64 exec, s[100:101]
	v_mul_lo_u32 v5, s18, v5
	v_mul_lo_u32 v7, s19, v3
	v_mad_u64_u32 v[64:65], s[22:23], s18, v3, 0
	v_add3_u32 v65, v65, v5, v7
	v_lshl_add_u64 v[64:65], v[64:65], 2, s[20:21]
	v_mov_b32_e32 v13, v1
	v_add_u32_e32 v3, s0, v57
	v_lshl_add_u64 v[64:65], v[64:65], 0, v[12:13]
	s_mov_b32 m0, s27
	v_ashrrev_i32_e32 v5, 31, v3
	s_mov_b64 exec, s[98:99]
	s_cbranch_execz .Lcv_sk_38
	global_load_lds_dwordx4 v[64:65], off nt
.Lcv_sk_38:
	s_mov_b64 exec, s[100:101]
	v_mul_lo_u32 v5, s18, v5
	v_mul_lo_u32 v7, s19, v3
	v_mad_u64_u32 v[64:65], s[18:19], s18, v3, 0
	v_add3_u32 v65, v65, v5, v7
	v_lshl_add_u64 v[64:65], v[64:65], 2, s[20:21]
	v_mov_b32_e32 v15, v1
	v_lshl_add_u64 v[64:65], v[64:65], 0, v[14:15]
	s_add_i32 m0, s26, s87
	s_cmp_ge_i32 s79, s42
	s_mov_b64 exec, s[98:99]
	s_cbranch_execz .Lcv_sk_39
	global_load_lds_dwordx4 v[64:65], off nt
.Lcv_sk_39:
	s_mov_b64 exec, s[100:101]
	s_cselect_b32 s19, s49, 0x2680
	s_add_i32 s19, s19, s79
	s_cmpk_gt_i32 s19, 0x37f
	s_mov_b64 s[24:25], -1
	s_cbranch_scc0 .LBB0_1319
	s_cmpk_gt_u32 s19, 0x47f
	s_cbranch_scc0 .LBB0_1316
	s_cmpk_gt_u32 s19, 0x67f
	s_cbranch_scc0 .LBB0_1313
	s_cmpk_gt_u32 s19, 0x467f
	s_mov_b64 s[20:21], -1
	s_cbranch_scc0 .LBB0_1310
	s_add_i32 s0, s19, 0xffffb980
	s_lshr_b32 s0, s0, 7
	s_lshl_b32 s18, s19, 7
	s_lshl_b32 s20, s19, 4
	s_and_b32 s18, s18, 0x380
	s_and_b32 s26, s20, 0x780
	s_lshl_b64 s[20:21], s[0:1], 22
	s_add_u32 s22, s10, s20
	s_addc_u32 s23, s11, s21
	s_mov_b64 s[20:21], 0

.LBB0_1407:
	s_ashr_i32 s23, s22, 31
	s_lshl_b64 s[22:23], s[22:23], 2
	v_add_u32_e32 v3, s0, v50
	s_add_u32 s20, s20, s22
	v_ashrrev_i32_e32 v5, 31, v3
	s_addc_u32 s21, s21, s23
	v_mul_lo_u32 v5, s18, v5
	v_mul_lo_u32 v7, s19, v3
	v_mad_u64_u32 v[64:65], s[22:23], s18, v3, 0
	v_add3_u32 v65, v65, v5, v7
	v_lshl_add_u64 v[64:65], v[64:65], 2, s[20:21]
	v_add_u32_e32 v3, s0, v51
	s_mov_b32 m0, s37
	v_lshl_add_u64 v[64:65], v[64:65], 0, v[0:1]
	v_ashrrev_i32_e32 v5, 31, v3
	s_mov_b64 exec, s[98:99]
	s_cbranch_execz .Lcv_sk_40
	global_load_lds_dwordx4 v[64:65], off nt
.Lcv_sk_40:
	s_mov_b64 exec, s[100:101]
	v_mul_lo_u32 v5, s18, v5
	v_mul_lo_u32 v7, s19, v3
	v_mad_u64_u32 v[64:65], s[22:23], s18, v3, 0
	v_add3_u32 v65, v65, v5, v7
	v_lshl_add_u64 v[64:65], v[64:65], 2, s[20:21]
	v_mov_b32_e32 v3, v1
	v_lshl_add_u64 v[64:65], v[64:65], 0, v[2:3]
	v_add_u32_e32 v3, s0, v52
	s_mov_b32 m0, s36
	v_ashrrev_i32_e32 v5, 31, v3
	s_mov_b64 exec, s[98:99]
	s_cbranch_execz .Lcv_sk_41
	global_load_lds_dwordx4 v[64:65], off nt
.Lcv_sk_41:
	s_mov_b64 exec, s[100:101]
	v_mul_lo_u32 v5, s18, v5
	v_mul_lo_u32 v7, s19, v3
	v_mad_u64_u32 v[64:65], s[22:23], s18, v3, 0
	v_add3_u32 v65, v65, v5, v7
	v_lshl_add_u64 v[64:65], v[64:65], 2, s[20:21]
	v_mov_b32_e32 v5, v1
	v_add_u32_e32 v3, s0, v53
	v_lshl_add_u64 v[64:65], v[64:65], 0, v[4:5]
	s_mov_b32 m0, s84
	v_ashrrev_i32_e32 v5, 31, v3
	s_mov_b64 exec, s[98:99]
	s_cbranch_execz .Lcv_sk_42
	global_load_lds_dwordx4 v[64:65], off nt
.Lcv_sk_42:
	s_mov_b64 exec, s[100:101]
	v_mul_lo_u32 v5, s18, v5
	v_mul_lo_u32 v7, s19, v3
	v_mad_u64_u32 v[64:65], s[22:23], s18, v3, 0
	v_add3_u32 v65, v65, v5, v7
	v_lshl_add_u64 v[64:65], v[64:65], 2, s[20:21]
	v_mov_b32_e32 v7, v1
	v_add_u32_e32 v3, s0, v54
	v_lshl_add_u64 v[64:65], v[64:65], 0, v[6:7]
	s_mov_b32 m0, s79
	v_ashrrev_i32_e32 v5, 31, v3
	s_mov_b64 exec, s[98:99]
	s_cbranch_execz .Lcv_sk_43
	global_load_lds_dwordx4 v[64:65], off nt
.Lcv_sk_43:
	s_mov_b64 exec, s[100:101]
	v_mul_lo_u32 v5, s18, v5
	v_mul_lo_u32 v7, s19, v3
	v_mad_u64_u32 v[64:65], s[22:23], s18, v3, 0
	v_add3_u32 v65, v65, v5, v7
	v_lshl_add_u64 v[64:65], v[64:65], 2, s[20:21]
	v_mov_b32_e32 v9, v1
	v_add_u32_e32 v3, s0, v55
	v_lshl_add_u64 v[64:65], v[64:65], 0, v[8:9]
	s_mov_b32 m0, s78
	v_ashrrev_i32_e32 v5, 31, v3
	s_mov_b64 exec, s[98:99]
	s_cbranch_execz .Lcv_sk_44
	global_load_lds_dwordx4 v[64:65], off nt
.Lcv_sk_44:
	s_mov_b64 exec, s[100:101]
	v_mul_lo_u32 v5, s18, v5
	v_mul_lo_u32 v7, s19, v3
	v_mad_u64_u32 v[64:65], s[22:23], s18, v3, 0
	v_add3_u32 v65, v65, v5, v7
	v_lshl_add_u64 v[64:65], v[64:65], 2, s[20:21]
	v_mov_b32_e32 v11, v1
	v_add_u32_e32 v3, s0, v56
	v_lshl_add_u64 v[64:65], v[64:65], 0, v[10:11]
	s_mov_b32 m0, s77
	v_ashrrev_i32_e32 v5, 31, v3
	s_mov_b64 exec, s[98:99]
	s_cbranch_execz .Lcv_sk_45
	global_load_lds_dwordx4 v[64:65], off nt

; __device__ __forceinline__ ConvJob conv_job(const Ctx& c, int t) {
;     ...
;     if (i < CV_IN) { const int kb = i % 16, cb = i / 16; j.src = c.in[4]; j.ld = NIN; j.k0 = kb * 128; j.col0 = cb * 128; j.dst = WSP(bf16, WS_WIN); j.dK = 2048; j.drow0 = cb * 128; return j; }
;     i -= CV_IN;
;     if (i < CV_OUT) { const int kb = i % 16, cb = i / 16; j.src = c.in[8]; j.ld = 2048; j.k0 = kb * 128; j.col0 = cb * 128; j.dst = WSP(bf16, WS_WOUT); j.dK = 2048; j.drow0 = cb * 128; return j; }
;     i -= CV_OUT;
;     if (i < CV_GLU) { const int kb = i % 16, cb = i / 16; j.src = c.in[17]; j.ld = 4096; j.k0 = kb * 128; j.col0 = cb * 128; j.dst = WSP(bf16, WS_WGLU); j.dK = 2048; j.drow0 = cb < 16 ? cb * 256 : (cb - 16) * 256 + 128; return j; }
;     i -= CV_GLU;
;     if (i < CV_GU) { const int kb = i % 16, cb = (i / 16) % 8, gu = (i / 128) % 2, le = i / 256;
;         j.src = (gu ? c.in[23] : c.in[22]) + (size_t)le * 2048 * 1024; j.ld = 1024; j.k0 = kb * 128; j.col0 = cb * 128; j.dst = WSP(bf16, WS_WGU) + (size_t)le * 2048 * 2048; j.dK = 2048; j.drow0 = cb * 256 + gu * 128; return j; }
;     i -= CV_GU;
;     { const int kb = i % 8, cb = (i / 8) % 16, le = i / 128;
;         j.src = c.in[24] + (size_t)le * 1024 * 2048; j.ld = 2048; j.k0 = kb * 128; j.col0 = cb * 128; j.dst = WSP(bf16, WS_WD) + (size_t)le * 2048 * 1024; j.dK = 1024; j.drow0 = cb * 128; return j; }
.Lcv_sk_46:
	s_mov_b64 exec, s[100:101]
	v_mul_lo_u32 v5, s18, v5
	v_mul_lo_u32 v7, s19, v3
	v_mad_u64_u32 v[64:65], s[18:19], s18, v3, 0
	v_add3_u32 v65, v65, v5, v7
	v_lshl_add_u64 v[64:65], v[64:65], 2, s[20:21]
	v_mov_b32_e32 v15, v1
	v_lshl_add_u64 v[64:65], v[64:65], 0, v[14:15]
	s_add_i32 m0, s26, s61
	s_cmp_lt_i32 s75, s43
	s_mov_b64 exec, s[98:99]
	s_cbranch_execz .Lcv_sk_47
	global_load_lds_dwordx4 v[64:65], off nt
.Lcv_sk_47:
	s_mov_b64 exec, s[100:101]
	s_cselect_b32 s19, s41, s42
	s_add_i32 s19, s19, s75
	s_cmpk_gt_i32 s19, 0x37f
	s_mov_b64 s[24:25], -1
	s_cbranch_scc0 .LBB0_1421
	s_cmpk_gt_u32 s19, 0x47f
	s_cbranch_scc0 .LBB0_1418
	s_cmpk_gt_u32 s19, 0x67f
	s_cbranch_scc0 .LBB0_1415
	s_cmpk_gt_u32 s19, 0x467f
	s_mov_b64 s[20:21], -1
	s_cbranch_scc0 .LBB0_1412
	s_add_i32 s0, s19, 0xffffb980
	s_lshr_b32 s0, s0, 7
	s_lshl_b32 s18, s19, 7
	s_lshl_b32 s20, s19, 4
	s_and_b32 s18, s18, 0x380
	s_and_b32 s26, s20, 0x780
	s_lshl_b64 s[20:21], s[0:1], 22
	s_add_u32 s22, s10, s20
	s_addc_u32 s23, s11, s21
	s_mov_b64 s[20:21], 0

; __device__ __forceinline__ ConvJob conv_job(const Ctx& c, int t) {
;     ...
;     if (i < CV_IN) { const int kb = i % 16, cb = i / 16; j.src = c.in[4]; j.ld = NIN; j.k0 = kb * 128; j.col0 = cb * 128; j.dst = WSP(bf16, WS_WIN); j.dK = 2048; j.drow0 = cb * 128; return j; }
;     i -= CV_IN;
;     if (i < CV_OUT) { const int kb = i % 16, cb = i / 16; j.src = c.in[8]; j.ld = 2048; j.k0 = kb * 128; j.col0 = cb * 128; j.dst = WSP(bf16, WS_WOUT); j.dK = 2048; j.drow0 = cb * 128; return j; }
;     i -= CV_OUT;
;     if (i < CV_GLU) { const int kb = i % 16, cb = i / 16; j.src = c.in[17]; j.ld = 4096; j.k0 = kb * 128; j.col0 = cb * 128; j.dst = WSP(bf16, WS_WGLU); j.dK = 2048; j.drow0 = cb < 16 ? cb * 256 : (cb - 16) * 256 + 128; return j; }
;     i -= CV_GLU;
;     if (i < CV_GU) { const int kb = i % 16, cb = (i / 16) % 8, gu = (i / 128) % 2, le = i / 256;
;         j.src = (gu ? c.in[23] : c.in[22]) + (size_t)le * 2048 * 1024; j.ld = 1024; j.k0 = kb * 128; j.col0 = cb * 128; j.dst = WSP(bf16, WS_WGU) + (size_t)le * 2048 * 2048; j.dK = 2048; j.drow0 = cb * 256 + gu * 128; return j; }
;     i -= CV_GU;
;     { const int kb = i % 8, cb = (i / 8) % 16, le = i / 128;
;         j.src = c.in[24] + (size_t)le * 1024 * 2048; j.ld = 2048; j.k0 = kb * 128; j.col0 = cb * 128; j.dst = WSP(bf16, WS_WD) + (size_t)le * 2048 * 1024; j.dK = 1024; j.drow0 = cb * 128; return j; }
.LBB0_1946:
	s_ashr_i32 s25, s24, 31
	s_lshl_b64 s[24:25], s[24:25], 2
	v_add_u32_e32 v3, s14, v50
	s_add_u32 s22, s22, s24
	v_ashrrev_i32_e32 v5, 31, v3
	s_addc_u32 s23, s23, s25
	v_mul_lo_u32 v5, s20, v5
	v_mul_lo_u32 v7, s21, v3
	v_mad_u64_u32 v[64:65], s[24:25], s20, v3, 0
	v_add3_u32 v65, v65, v5, v7
	v_lshl_add_u64 v[64:65], v[64:65], 2, s[22:23]
	v_add_u32_e32 v3, s14, v51
	s_mov_b32 m0, s84
	v_lshl_add_u64 v[64:65], v[64:65], 0, v[0:1]
	v_ashrrev_i32_e32 v5, 31, v3
	s_mov_b64 exec, s[98:99]
	s_cbranch_execz .Lcv_sk_48
	global_load_lds_dwordx4 v[64:65], off nt
.Lcv_sk_48:
	s_mov_b64 exec, s[100:101]
	v_mul_lo_u32 v5, s20, v5
	v_mul_lo_u32 v7, s21, v3
	v_mad_u64_u32 v[64:65], s[24:25], s20, v3, 0
	v_add3_u32 v65, v65, v5, v7
	v_lshl_add_u64 v[64:65], v[64:65], 2, s[22:23]
	v_mov_b32_e32 v3, v1
	v_lshl_add_u64 v[64:65], v[64:65], 0, v[2:3]
	v_add_u32_e32 v3, s14, v52
	s_mov_b32 m0, s81
	v_ashrrev_i32_e32 v5, 31, v3
	s_mov_b64 exec, s[98:99]
	s_cbranch_execz .Lcv_sk_49
	global_load_lds_dwordx4 v[64:65], off nt
.Lcv_sk_49:
	s_mov_b64 exec, s[100:101]
	v_mul_lo_u32 v5, s20, v5
	v_mul_lo_u32 v7, s21, v3
	v_mad_u64_u32 v[64:65], s[24:25], s20, v3, 0
	v_add3_u32 v65, v65, v5, v7
	v_lshl_add_u64 v[64:65], v[64:65], 2, s[22:23]
	v_mov_b32_e32 v5, v1
	v_add_u32_e32 v3, s14, v53
	v_lshl_add_u64 v[64:65], v[64:65], 0, v[4:5]
	s_mov_b32 m0, s80
	v_ashrrev_i32_e32 v5, 31, v3
	s_mov_b64 exec, s[98:99]
	s_cbranch_execz .Lcv_sk_50
	global_load_lds_dwordx4 v[64:65], off nt
.Lcv_sk_50:
	s_mov_b64 exec, s[100:101]
	v_mul_lo_u32 v5, s20, v5
	v_mul_lo_u32 v7, s21, v3
	v_mad_u64_u32 v[64:65], s[24:25], s20, v3, 0
	v_add3_u32 v65, v65, v5, v7
	v_lshl_add_u64 v[64:65], v[64:65], 2, s[22:23]
	v_mov_b32_e32 v7, v1
	v_add_u32_e32 v3, s14, v54
	v_lshl_add_u64 v[64:65], v[64:65], 0, v[6:7]
	s_mov_b32 m0, s79
	v_ashrrev_i32_e32 v5, 31, v3
	s_mov_b64 exec, s[98:99]
	s_cbranch_execz .Lcv_sk_51
	global_load_lds_dwordx4 v[64:65], off nt
.Lcv_sk_51:
	s_mov_b64 exec, s[100:101]
	v_mul_lo_u32 v5, s20, v5
	v_mul_lo_u32 v7, s21, v3
	v_mad_u64_u32 v[64:65], s[24:25], s20, v3, 0
	v_add3_u32 v65, v65, v5, v7
	v_lshl_add_u64 v[64:65], v[64:65], 2, s[22:23]
	v_mov_b32_e32 v9, v1
	v_add_u32_e32 v3, s14, v55
	v_lshl_add_u64 v[64:65], v[64:65], 0, v[8:9]
	s_mov_b32 m0, s78
	v_ashrrev_i32_e32 v5, 31, v3
	s_mov_b64 exec, s[98:99]
	s_cbranch_execz .Lcv_sk_52
	global_load_lds_dwordx4 v[64:65], off nt
.Lcv_sk_52:
	s_mov_b64 exec, s[100:101]
	v_mul_lo_u32 v5, s20, v5
	v_mul_lo_u32 v7, s21, v3
	v_mad_u64_u32 v[64:65], s[24:25], s20, v3, 0
	v_add3_u32 v65, v65, v5, v7
	v_lshl_add_u64 v[64:65], v[64:65], 2, s[22:23]
	v_mov_b32_e32 v11, v1
	v_add_u32_e32 v3, s14, v56
	v_lshl_add_u64 v[64:65], v[64:65], 0, v[10:11]
	s_mov_b32 m0, s77
	v_ashrrev_i32_e32 v5, 31, v3
	s_mov_b64 exec, s[98:99]
	s_cbranch_execz .Lcv_sk_53
	global_load_lds_dwordx4 v[64:65], off nt
.Lcv_sk_53:
	s_mov_b64 exec, s[100:101]
	v_mul_lo_u32 v5, s20, v5
	v_mul_lo_u32 v7, s21, v3
	v_mad_u64_u32 v[64:65], s[24:25], s20, v3, 0
	v_add3_u32 v65, v65, v5, v7
	v_lshl_add_u64 v[64:65], v[64:65], 2, s[22:23]
	v_mov_b32_e32 v13, v1
	v_add_u32_e32 v3, s14, v57
	v_lshl_add_u64 v[64:65], v[64:65], 0, v[12:13]
	s_mov_b32 m0, s29
	v_ashrrev_i32_e32 v5, 31, v3
	s_mov_b64 exec, s[98:99]
	s_cbranch_execz .Lcv_sk_54
	global_load_lds_dwordx4 v[64:65], off nt
.Lcv_sk_54:
	s_mov_b64 exec, s[100:101]
	v_mul_lo_u32 v5, s20, v5
	v_mul_lo_u32 v7, s21, v3
	v_mad_u64_u32 v[64:65], s[20:21], s20, v3, 0
	v_add3_u32 v65, v65, v5, v7
	v_lshl_add_u64 v[64:65], v[64:65], 2, s[22:23]
	v_mov_b32_e32 v15, v1
	v_lshl_add_u64 v[64:65], v[64:65], 0, v[14:15]
	s_add_i32 m0, s28, s49
	s_cmpk_lt_i32 s74, 0x1300
	s_mov_b64 exec, s[98:99]
	s_cbranch_execz .Lcv_sk_55
	global_load_lds_dwordx4 v[64:65], off nt
.Lcv_sk_55:
	s_mov_b64 exec, s[100:101]
	s_cselect_b32 s21, s73, 0xffffed00
	s_add_i32 s21, s21, s74
	s_cmpk_gt_i32 s21, 0x37f
	s_mov_b64 s[26:27], -1
	s_cbranch_scc0 .LBB0_1960
	s_cmpk_gt_u32 s21, 0x47f
	s_cbranch_scc0 .LBB0_1957
	s_cmpk_gt_u32 s21, 0x67f
	s_cbranch_scc0 .LBB0_1954
	s_cmpk_gt_u32 s21, 0x467f
	s_mov_b64 s[22:23], -1
	s_cbranch_scc0 .LBB0_1951
	s_add_i32 s14, s21, 0xffffb980
	s_lshr_b32 s14, s14, 7
	s_and_b32 s20, s71, 0x380
	s_and_b32 s28, s69, 0x780
	s_lshl_b64 s[22:23], s[14:15], 22
	s_add_u32 s24, s63, s22
	s_addc_u32 s25, s66, s23
	s_mov_b64 s[22:23], 0

.LBB0_2270:
	s_ashr_i32 s25, s24, 31
	s_lshl_b64 s[24:25], s[24:25], 2
	v_add_u32_e32 v3, s0, v50
	s_add_u32 s22, s22, s24
	v_ashrrev_i32_e32 v5, 31, v3
	s_addc_u32 s23, s23, s25
	v_mul_lo_u32 v5, s20, v5
	v_mul_lo_u32 v7, s21, v3
	v_mad_u64_u32 v[64:65], s[24:25], s20, v3, 0
	v_add3_u32 v65, v65, v5, v7
	v_lshl_add_u64 v[64:65], v[64:65], 2, s[22:23]
	v_add_u32_e32 v3, s0, v51
	s_mov_b32 m0, s86
	v_lshl_add_u64 v[64:65], v[64:65], 0, v[0:1]
	v_ashrrev_i32_e32 v5, 31, v3
	s_mov_b64 exec, s[98:99]
	s_cbranch_execz .Lcv_sk_56
	global_load_lds_dwordx4 v[64:65], off nt
.Lcv_sk_56:
	s_mov_b64 exec, s[100:101]
	v_mul_lo_u32 v5, s20, v5
	v_mul_lo_u32 v7, s21, v3
	v_mad_u64_u32 v[64:65], s[24:25], s20, v3, 0
	v_add3_u32 v65, v65, v5, v7
	v_lshl_add_u64 v[64:65], v[64:65], 2, s[22:23]
	v_mov_b32_e32 v3, v1
	v_lshl_add_u64 v[64:65], v[64:65], 0, v[2:3]
	v_add_u32_e32 v3, s0, v52
	s_mov_b32 m0, s85
	v_ashrrev_i32_e32 v5, 31, v3
	s_mov_b64 exec, s[98:99]
	s_cbranch_execz .Lcv_sk_57
	global_load_lds_dwordx4 v[64:65], off nt

.Lcv_sk_58:
	s_mov_b64 exec, s[100:101]
	v_mul_lo_u32 v5, s20, v5
	v_mul_lo_u32 v7, s21, v3
	v_mad_u64_u32 v[64:65], s[24:25], s20, v3, 0
	v_add3_u32 v65, v65, v5, v7
	v_lshl_add_u64 v[64:65], v[64:65], 2, s[22:23]
	v_mov_b32_e32 v7, v1
	v_add_u32_e32 v3, s0, v54
	v_lshl_add_u64 v[64:65], v[64:65], 0, v[6:7]
	s_mov_b32 m0, s81
	v_ashrrev_i32_e32 v5, 31, v3
	s_mov_b64 exec, s[98:99]
	s_cbranch_execz .Lcv_sk_59
	global_load_lds_dwordx4 v[64:65], off nt
.Lcv_sk_59:
	s_mov_b64 exec, s[100:101]
	v_mul_lo_u32 v5, s20, v5
	v_mul_lo_u32 v7, s21, v3
	v_mad_u64_u32 v[64:65], s[24:25], s20, v3, 0
	v_add3_u32 v65, v65, v5, v7
	v_lshl_add_u64 v[64:65], v[64:65], 2, s[22:23]
	v_mov_b32_e32 v9, v1
	v_add_u32_e32 v3, s0, v55
	v_lshl_add_u64 v[64:65], v[64:65], 0, v[8:9]
	s_mov_b32 m0, s80
	v_ashrrev_i32_e32 v5, 31, v3
	s_mov_b64 exec, s[98:99]
	s_cbranch_execz .Lcv_sk_60
	global_load_lds_dwordx4 v[64:65], off nt
.Lcv_sk_60:
	s_mov_b64 exec, s[100:101]
	v_mul_lo_u32 v5, s20, v5
	v_mul_lo_u32 v7, s21, v3
	v_mad_u64_u32 v[64:65], s[24:25], s20, v3, 0
	v_add3_u32 v65, v65, v5, v7
	v_lshl_add_u64 v[64:65], v[64:65], 2, s[22:23]
	v_mov_b32_e32 v11, v1
	v_add_u32_e32 v3, s0, v56
	v_lshl_add_u64 v[64:65], v[64:65], 0, v[10:11]
	s_mov_b32 m0, s79
	v_ashrrev_i32_e32 v5, 31, v3
	s_mov_b64 exec, s[98:99]
	s_cbranch_execz .Lcv_sk_61
	global_load_lds_dwordx4 v[64:65], off nt

; __device__ __forceinline__ ConvJob conv_job(const Ctx& c, int t) {
;     ...
;     if (i < CV_IN) { const int kb = i % 16, cb = i / 16; j.src = c.in[4]; j.ld = NIN; j.k0 = kb * 128; j.col0 = cb * 128; j.dst = WSP(bf16, WS_WIN); j.dK = 2048; j.drow0 = cb * 128; return j; }
;     i -= CV_IN;
;     if (i < CV_OUT) { const int kb = i % 16, cb = i / 16; j.src = c.in[8]; j.ld = 2048; j.k0 = kb * 128; j.col0 = cb * 128; j.dst = WSP(bf16, WS_WOUT); j.dK = 2048; j.drow0 = cb * 128; return j; }
;     i -= CV_OUT;
;     if (i < CV_GLU) { const int kb = i % 16, cb = i / 16; j.src = c.in[17]; j.ld = 4096; j.k0 = kb * 128; j.col0 = cb * 128; j.dst = WSP(bf16, WS_WGLU); j.dK = 2048; j.drow0 = cb < 16 ? cb * 256 : (cb - 16) * 256 + 128; return j; }
;     i -= CV_GLU;
;     if (i < CV_GU) { const int kb = i % 16, cb = (i / 16) % 8, gu = (i / 128) % 2, le = i / 256;
;         j.src = (gu ? c.in[23] : c.in[22]) + (size_t)le * 2048 * 1024; j.ld = 1024; j.k0 = kb * 128; j.col0 = cb * 128; j.dst = WSP(bf16, WS_WGU) + (size_t)le * 2048 * 2048; j.dK = 2048; j.drow0 = cb * 256 + gu * 128; return j; }
;     i -= CV_GU;
;     { const int kb = i % 8, cb = (i / 8) % 16, le = i / 128;
;         j.src = c.in[24] + (size_t)le * 1024 * 2048; j.ld = 2048; j.k0 = kb * 128; j.col0 = cb * 128; j.dst = WSP(bf16, WS_WD) + (size_t)le * 2048 * 1024; j.dK = 1024; j.drow0 = cb * 128; return j; }
.Lcv_sk_62:
	s_mov_b64 exec, s[100:101]
	v_mul_lo_u32 v5, s20, v5
	v_mul_lo_u32 v7, s21, v3
	v_mad_u64_u32 v[64:65], s[20:21], s20, v3, 0
	v_add3_u32 v65, v65, v5, v7
	v_lshl_add_u64 v[64:65], v[64:65], 2, s[22:23]
	v_mov_b32_e32 v15, v1
	v_lshl_add_u64 v[64:65], v[64:65], 0, v[14:15]
	s_add_i32 m0, s28, s61
	s_cmp_ge_i32 s77, s33
	s_mov_b64 exec, s[98:99]
	s_cbranch_execz .Lcv_sk_63
	global_load_lds_dwordx4 v[64:65], off nt
.Lcv_sk_63:
	s_mov_b64 exec, s[100:101]
	s_cselect_b32 s21, s38, 0x5680
	s_add_i32 s21, s21, s77
	s_cmpk_gt_i32 s21, 0x37f
	s_mov_b64 s[26:27], -1
	s_cbranch_scc0 .LBB0_2284
	s_cmpk_gt_u32 s21, 0x47f
	s_cbranch_scc0 .LBB0_2281
	s_cmpk_gt_u32 s21, 0x67f
	s_cbranch_scc0 .LBB0_2278
	s_cmpk_gt_u32 s21, 0x467f
	s_mov_b64 s[22:23], -1
	s_cbranch_scc0 .LBB0_2275
	s_add_i32 s0, s21, 0xffffb980
	s_lshr_b32 s0, s0, 7
	s_lshl_b32 s20, s21, 7
	s_lshl_b32 s22, s21, 4
	s_and_b32 s20, s20, 0x380
	s_and_b32 s28, s22, 0x780
	s_lshl_b64 s[22:23], s[0:1], 22
	s_add_u32 s24, s73, s22
	s_addc_u32 s25, s74, s23
	s_mov_b64 s[22:23], 0

.LBB0_2372:
	s_ashr_i32 s25, s24, 31
	s_lshl_b64 s[24:25], s[24:25], 2
	v_add_u32_e32 v3, s0, v50
	s_add_u32 s22, s22, s24
	v_ashrrev_i32_e32 v5, 31, v3
	s_addc_u32 s23, s23, s25
	v_mul_lo_u32 v5, s20, v5
	v_mul_lo_u32 v7, s21, v3
	v_mad_u64_u32 v[64:65], s[24:25], s20, v3, 0
	v_add3_u32 v65, v65, v5, v7
	v_lshl_add_u64 v[64:65], v[64:65], 2, s[22:23]
	v_add_u32_e32 v3, s0, v51
	s_mov_b32 m0, s80
	v_lshl_add_u64 v[64:65], v[64:65], 0, v[0:1]
	v_ashrrev_i32_e32 v5, 31, v3
	s_mov_b64 exec, s[98:99]
	s_cbranch_execz .Lcv_sk_64
	global_load_lds_dwordx4 v[64:65], off nt
.Lcv_sk_64:
	s_mov_b64 exec, s[100:101]
	v_mul_lo_u32 v5, s20, v5
	v_mul_lo_u32 v7, s21, v3
	v_mad_u64_u32 v[64:65], s[24:25], s20, v3, 0
	v_add3_u32 v65, v65, v5, v7
	v_lshl_add_u64 v[64:65], v[64:65], 2, s[22:23]
	v_mov_b32_e32 v3, v1
	v_lshl_add_u64 v[64:65], v[64:65], 0, v[2:3]
	v_add_u32_e32 v3, s0, v52
	s_mov_b32 m0, s79
	v_ashrrev_i32_e32 v5, 31, v3
	s_mov_b64 exec, s[98:99]
	s_cbranch_execz .Lcv_sk_65
	global_load_lds_dwordx4 v[64:65], off nt
.Lcv_sk_65:
	s_mov_b64 exec, s[100:101]
	v_mul_lo_u32 v5, s20, v5
	v_mul_lo_u32 v7, s21, v3
	v_mad_u64_u32 v[64:65], s[24:25], s20, v3, 0
	v_add3_u32 v65, v65, v5, v7
	v_lshl_add_u64 v[64:65], v[64:65], 2, s[22:23]
	v_mov_b32_e32 v5, v1
	v_add_u32_e32 v3, s0, v53
	v_lshl_add_u64 v[64:65], v[64:65], 0, v[4:5]
	s_mov_b32 m0, s78
	v_ashrrev_i32_e32 v5, 31, v3
	s_mov_b64 exec, s[98:99]
	s_cbranch_execz .Lcv_sk_66
	global_load_lds_dwordx4 v[64:65], off nt
.Lcv_sk_66:
	s_mov_b64 exec, s[100:101]
	v_mul_lo_u32 v5, s20, v5
	v_mul_lo_u32 v7, s21, v3
	v_mad_u64_u32 v[64:65], s[24:25], s20, v3, 0
	v_add3_u32 v65, v65, v5, v7
	v_lshl_add_u64 v[64:65], v[64:65], 2, s[22:23]
	v_mov_b32_e32 v7, v1
	v_add_u32_e32 v3, s0, v54
	v_lshl_add_u64 v[64:65], v[64:65], 0, v[6:7]
	s_mov_b32 m0, s77
	v_ashrrev_i32_e32 v5, 31, v3
	s_mov_b64 exec, s[98:99]
	s_cbranch_execz .Lcv_sk_67
	global_load_lds_dwordx4 v[64:65], off nt
.Lcv_sk_67:
	s_mov_b64 exec, s[100:101]
	v_mul_lo_u32 v5, s20, v5
	v_mul_lo_u32 v7, s21, v3
	v_mad_u64_u32 v[64:65], s[24:25], s20, v3, 0
	v_add3_u32 v65, v65, v5, v7
	v_lshl_add_u64 v[64:65], v[64:65], 2, s[22:23]
	v_mov_b32_e32 v9, v1
	v_add_u32_e32 v3, s0, v55
	v_lshl_add_u64 v[64:65], v[64:65], 0, v[8:9]
	s_mov_b32 m0, s76
	v_ashrrev_i32_e32 v5, 31, v3
	s_mov_b64 exec, s[98:99]
	s_cbranch_execz .Lcv_sk_68
	global_load_lds_dwordx4 v[64:65], off nt
.Lcv_sk_68:
	s_mov_b64 exec, s[100:101]
	v_mul_lo_u32 v5, s20, v5
	v_mul_lo_u32 v7, s21, v3
	v_mad_u64_u32 v[64:65], s[24:25], s20, v3, 0
	v_add3_u32 v65, v65, v5, v7
	v_lshl_add_u64 v[64:65], v[64:65], 2, s[22:23]
	v_mov_b32_e32 v11, v1
	v_add_u32_e32 v3, s0, v56
	v_lshl_add_u64 v[64:65], v[64:65], 0, v[10:11]
	s_mov_b32 m0, s75
	v_ashrrev_i32_e32 v5, 31, v3
	s_mov_b64 exec, s[98:99]
	s_cbranch_execz .Lcv_sk_69
	global_load_lds_dwordx4 v[64:65], off nt

; __device__ __forceinline__ ConvJob conv_job(const Ctx& c, int t) {
;     ...
;     if (i < CV_IN) { const int kb = i % 16, cb = i / 16; j.src = c.in[4]; j.ld = NIN; j.k0 = kb * 128; j.col0 = cb * 128; j.dst = WSP(bf16, WS_WIN); j.dK = 2048; j.drow0 = cb * 128; return j; }
;     i -= CV_IN;
;     if (i < CV_OUT) { const int kb = i % 16, cb = i / 16; j.src = c.in[8]; j.ld = 2048; j.k0 = kb * 128; j.col0 = cb * 128; j.dst = WSP(bf16, WS_WOUT); j.dK = 2048; j.drow0 = cb * 128; return j; }
;     i -= CV_OUT;
;     if (i < CV_GLU) { const int kb = i % 16, cb = i / 16; j.src = c.in[17]; j.ld = 4096; j.k0 = kb * 128; j.col0 = cb * 128; j.dst = WSP(bf16, WS_WGLU); j.dK = 2048; j.drow0 = cb < 16 ? cb * 256 : (cb - 16) * 256 + 128; return j; }
;     i -= CV_GLU;
;     if (i < CV_GU) { const int kb = i % 16, cb = (i / 16) % 8, gu = (i / 128) % 2, le = i / 256;
;         j.src = (gu ? c.in[23] : c.in[22]) + (size_t)le * 2048 * 1024; j.ld = 1024; j.k0 = kb * 128; j.col0 = cb * 128; j.dst = WSP(bf16, WS_WGU) + (size_t)le * 2048 * 2048; j.dK = 2048; j.drow0 = cb * 256 + gu * 128; return j; }
;     i -= CV_GU;
;     { const int kb = i % 8, cb = (i / 8) % 16, le = i / 128;
;         j.src = c.in[24] + (size_t)le * 1024 * 2048; j.ld = 2048; j.k0 = kb * 128; j.col0 = cb * 128; j.dst = WSP(bf16, WS_WD) + (size_t)le * 2048 * 1024; j.dK = 1024; j.drow0 = cb * 128; return j; }
.Lcv_sk_70:
	s_mov_b64 exec, s[100:101]
	v_mul_lo_u32 v5, s20, v5
	v_mul_lo_u32 v7, s21, v3
	v_mad_u64_u32 v[64:65], s[20:21], s20, v3, 0
	v_add3_u32 v65, v65, v5, v7
	v_lshl_add_u64 v[64:65], v[64:65], 2, s[22:23]
	v_mov_b32_e32 v15, v1
	v_lshl_add_u64 v[64:65], v[64:65], 0, v[14:15]
	s_add_i32 m0, s28, s53
	s_cmp_lt_i32 s73, s34
	s_mov_b64 exec, s[98:99]
	s_cbranch_execz .Lcv_sk_71
	global_load_lds_dwordx4 v[64:65], off nt
.Lcv_sk_71:
	s_mov_b64 exec, s[100:101]
	s_cselect_b32 s21, s31, s33
	s_add_i32 s21, s21, s73
	s_cmpk_gt_i32 s21, 0x37f
	s_mov_b64 s[26:27], -1
	s_cbranch_scc0 .LBB0_2386
	s_cmpk_gt_u32 s21, 0x47f
	s_cbranch_scc0 .LBB0_2383
	s_cmpk_gt_u32 s21, 0x67f
	s_cbranch_scc0 .LBB0_2380
	s_cmpk_gt_u32 s21, 0x467f
	s_mov_b64 s[22:23], -1
	s_cbranch_scc0 .LBB0_2377
	s_add_i32 s0, s21, 0xffffb980
	s_lshr_b32 s0, s0, 7
	s_lshl_b32 s20, s21, 7
	s_lshl_b32 s22, s21, 4
	s_and_b32 s20, s20, 0x380
	s_and_b32 s28, s22, 0x780
	s_lshl_b64 s[22:23], s[0:1], 22
	s_add_u32 s24, s69, s22
	s_addc_u32 s25, s70, s23
	s_mov_b64 s[22:23], 0
